# E27: E25 + compressed-attention (cmp2) tile loop: the 4 LDS-DMA issues moved below the first 6 ds_reads
# speedup vs baseline: 1.0016x; 1.0016x over previous
.LBB0_593:
	s_lshl_b32 s0, s33, 14
	s_add_i32 s0, s0, 0
	v_add_u32_e32 v0, s0, v140
	ds_read_b128 v[68:71], v0
	ds_read_b128 v[72:75], v0 offset:4096
	ds_read_b128 v[76:79], v197
	ds_read_b128 v[80:83], v197 offset:4096
	ds_read_b128 v[84:87], v0 offset:8192
	ds_read_b128 v[92:95], v0 offset:12288
	s_cmp_ge_u32 s3, s89
	s_cbranch_scc1 .Lc591_skip
	s_cmp_eq_u32 s33, 0
	s_cselect_b32 s98, 0x4000, 0
	s_cselect_b32 s99, s79, 0x8000
	s_add_i32 s98, s28, s98
	v_lshl_add_u64 v[240:241], v[130:131], 0, s[8:9]
	s_mov_b32 m0, s98
	s_nop 0
	global_load_lds_dwordx4 v[240:241], off
	v_lshl_add_u64 v[240:241], v[132:133], 0, s[8:9]
	s_add_i32 m0, s98, 0x400
	s_add_i32 s98, s28, s99
	global_load_lds_dwordx4 v[240:241], off
	v_lshl_add_u64 v[240:241], v[134:135], 0, s[8:9]
	s_mov_b32 m0, s98
	s_nop 0
	global_load_lds_dwordx4 v[240:241], off
	v_lshl_add_u64 v[240:241], v[136:137], 0, s[8:9]
	s_add_i32 m0, s98, 0x400
	s_nop 0
	global_load_lds_dwordx4 v[240:241], off
.Lc591_skip:
	s_waitcnt lgkmcnt(3)
	v_mfma_f32_16x16x32_bf16 v[88:91], v[68:71], v[76:79], 0
	s_waitcnt lgkmcnt(2)
	v_mfma_f32_16x16x32_bf16 v[68:71], v[68:71], v[80:83], 0
	v_add_u32_e32 v0, s0, v143
	ds_read_b128 v[202:205], v0
	ds_read_b128 v[206:209], v197 offset:1024
	ds_read_b128 v[210:213], v197 offset:5120
	v_mfma_f32_16x16x32_bf16 v[96:99], v[72:75], v[76:79], 0
	v_mfma_f32_16x16x32_bf16 v[72:75], v[72:75], v[80:83], 0
	s_waitcnt lgkmcnt(4)
	v_mfma_f32_16x16x32_bf16 v[214:217], v[84:87], v[76:79], 0
	ds_read_b128 v[218:221], v0 offset:4096
	v_mfma_f32_16x16x32_bf16 v[84:87], v[84:87], v[80:83], 0
	s_waitcnt lgkmcnt(4)
	v_mfma_f32_16x16x32_bf16 v[76:79], v[92:95], v[76:79], 0
	v_mfma_f32_16x16x32_bf16 v[80:83], v[92:95], v[80:83], 0
	ds_read_b128 v[92:95], v0 offset:8192
	s_waitcnt lgkmcnt(3)
	v_mfma_f32_16x16x32_bf16 v[88:91], v[202:205], v[206:209], v[88:91]
	s_waitcnt lgkmcnt(2)
	v_mfma_f32_16x16x32_bf16 v[68:71], v[202:205], v[210:213], v[68:71]
	ds_read_b128 v[202:205], v0 offset:12288
	v_add_u32_e32 v0, s0, v144
	s_waitcnt lgkmcnt(2)
	v_mfma_f32_16x16x32_bf16 v[96:99], v[218:221], v[206:209], v[96:99]
	v_mfma_f32_16x16x32_bf16 v[72:75], v[218:221], v[210:213], v[72:75]
	ds_read_b128 v[218:221], v0
	ds_read_b128 v[222:225], v197 offset:2048
	ds_read_b128 v[228:231], v197 offset:6144
	s_waitcnt lgkmcnt(4)
	v_mfma_f32_16x16x32_bf16 v[214:217], v[92:95], v[206:209], v[214:217]
	v_mfma_f32_16x16x32_bf16 v[84:87], v[92:95], v[210:213], v[84:87]
	ds_read_b128 v[92:95], v0 offset:4096
	s_waitcnt lgkmcnt(4)
	v_mfma_f32_16x16x32_bf16 v[76:79], v[202:205], v[206:209], v[76:79]
	ds_read_b128 v[206:209], v0 offset:8192
	v_mfma_f32_16x16x32_bf16 v[80:83], v[202:205], v[210:213], v[80:83]
	ds_read_b128 v[202:205], v0 offset:12288
	s_waitcnt lgkmcnt(4)
	v_mfma_f32_16x16x32_bf16 v[88:91], v[218:221], v[222:225], v[88:91]
	s_waitcnt lgkmcnt(3)
	v_mfma_f32_16x16x32_bf16 v[68:71], v[218:221], v[228:231], v[68:71]
	v_add_u32_e32 v0, s0, v145
	s_waitcnt lgkmcnt(2)
	v_mfma_f32_16x16x32_bf16 v[210:213], v[92:95], v[222:225], v[96:99]
	v_mfma_f32_16x16x32_bf16 v[72:75], v[92:95], v[228:231], v[72:75]
	ds_read_b128 v[92:95], v0
	ds_read_b128 v[218:221], v197 offset:3072
	ds_read_b128 v[232:235], v197 offset:7168
	s_waitcnt lgkmcnt(4)
	v_mfma_f32_16x16x32_bf16 v[214:217], v[206:209], v[222:225], v[214:217]
	v_mfma_f32_16x16x32_bf16 v[84:87], v[206:209], v[228:231], v[84:87]
	ds_read_b128 v[206:209], v0 offset:4096
	s_waitcnt lgkmcnt(4)
	v_mfma_f32_16x16x32_bf16 v[222:225], v[202:205], v[222:225], v[76:79]
	ds_read_b128 v[236:239], v0 offset:8192
	v_mfma_f32_16x16x32_bf16 v[202:205], v[202:205], v[228:231], v[80:83]
	s_waitcnt lgkmcnt(2)
	v_mfma_f32_16x16x32_bf16 v[80:83], v[92:95], v[232:235], v[68:71]
	s_nop 2
	ds_read_b128 v[68:71], v0 offset:12288
	v_mfma_f32_16x16x32_bf16 v[96:99], v[92:95], v[218:221], v[88:91]
	s_waitcnt lgkmcnt(2)
	v_mfma_f32_16x16x32_bf16 v[92:95], v[206:209], v[218:221], v[210:213]
	v_mfma_f32_16x16x32_bf16 v[76:79], v[206:209], v[232:235], v[72:75]
	s_waitcnt lgkmcnt(1)
	v_mfma_f32_16x16x32_bf16 v[88:91], v[236:239], v[218:221], v[214:217]
	v_mfma_f32_16x16x32_bf16 v[72:75], v[236:239], v[232:235], v[84:87]
	s_waitcnt lgkmcnt(0)
	v_mfma_f32_16x16x32_bf16 v[84:87], v[68:71], v[218:221], v[222:225]
	v_mfma_f32_16x16x32_bf16 v[68:71], v[68:71], v[232:235], v[202:205]
	s_nop 2
	v_add_u32_e32 v204, s2, v195
	v_subrev_u32_e32 v205, 31, v204
	v_cmp_lt_i32_e32 vcc, -1, v205
	v_mov_b32_e32 v202, 0xff800000
	v_mov_b32_e32 v203, 0xff800000
	s_and_saveexec_b64 s[0:1], vcc
	s_cbranch_execz .LBB0_595
	v_min_u32_e32 v0, 0x7f, v205
	v_lshl_add_u32 v0, v0, 2, v196
	ds_read_b32 v203, v0
	s_waitcnt lgkmcnt(0)
	v_fmac_f32_e32 v203, 0x3fb8aa3b, v96
